# PEER U row prefetch: addresses formed on the scalar unit (table base in s[100:101], per-lane offset v224) instead of a 64-bit VALU add per row
# speedup vs baseline: 1.0022x; 1.0015x over previous
; #define LAS __attribute__((address_space(3)))
; #define U_RANGE(T, P, RLO, RHI, BLO, BHI) PL_RANGE4(T, P, RLO, RHI, BLO, BHI)
; __device__ __forceinline__ void peer_unit(Frame& F, const Args& a, int layer, int unit, bool last) {
;     ...
;     for (int it = 0; it < 16; ++it) {
;         const v4u se = se_pf;
;         if (it < 15) se_pf = *(const v4u*)(SELW + (tokb + it + 1) * 256 + 4 * lane);
;         const unsigned b0 = se.x >> 12, b1 = se.z >> 12;
;         unsigned pos0 = 0u, pos1 = 0u, base = 0u, pk = 0u;
; #pragma unroll
;         for (unsigned k = 0; k < 4; ++k) {
;             const unsigned long long m0 = __builtin_amdgcn_ballot_w64(b0 == k), m1 = __builtin_amdgcn_ballot_w64(b1 == k);
;             const unsigned below = __builtin_amdgcn_mbcnt_hi((unsigned)(m0 >> 32), __builtin_amdgcn_mbcnt_lo((unsigned)m0, 0u)) + __builtin_amdgcn_mbcnt_hi((unsigned)(m1 >> 32), __builtin_amdgcn_mbcnt_lo((unsigned)m1, 0u));
;             if (b0 == k) pos0 = base + below;
;             if (b1 == k) pos1 = base + below + (b0 == k ? 1u : 0u);
;             base += (unsigned)__builtin_popcountll(m0) + (unsigned)__builtin_popcountll(m1);
;             if (k < 3) pk |= base << (8 * k);
;         }
;     ...
;         pos0 = 2 * lane; pos1 = 2 * lane + 1;
;     ...
;         *(LAS v2u*)(sSort + 2 * pos0) = (v2u){se.x, se.y}; *(LAS v2u*)(sSort + 2 * pos1) = (v2u){se.z, se.w};
;         asm volatile("" ::: "memory");
;         const v2u so0 = *(const LAS v2u*)(sSort + 4 * lane), so1 = *(const LAS v2u*)(sSort + 4 * lane + 2); const v4u so = (v4u){so0.x, so0.y, so1.x, so1.y};
;         asm volatile("" ::: "memory");
;         sIdx[it * 64 + lane] = (so0.x & 0xffffu) | (so1.x << 16);
;         (void)so;
;         { const unsigned g0 = so0.y, g1 = so1.y; sCoef[it * 128 + 2 * lane] = __uint_as_float(g0); sCoef[it * 128 + 2 * lane + 1] = __uint_as_float(g1); }
;         if (lane == it) cnts = pk;
;     }
;     ...
;     for (int ps = DBG_U0; ps < UPASS; ++ps) {
;         int lt = 0, lb, lbh; { U_RANGE(lt, ps, r0, r1, b0_, b1_); lb = b0_; lbh = b1_; (void)r0; (void)r1; }
;         unsigned seL = sIdx[lane];
;         long xlo = 0, xhi = 0; const bool dsel = ((lane >> 2) & 3) == (lane >> 4); const unsigned char* N8 = (const unsigned char*)(F.ws + WS_N8); v4u nnx = *(const v4u*)(N8 + tokb * 1024 + 16 * lane);
;         int ct, cb, crl = 0, crh = 0, cbl = 0;
.LBB0_1726:
	s_waitcnt vmcnt(0)
	v_mov_b64_e32 v[16:17], v[4:5]
	v_mov_b64_e32 v[14:15], v[2:3]
	global_load_dwordx4 v[2:5], v[6:7], off
	v_cmp_gt_u32_e32 vcc, s9, v14
	v_cmp_gt_u32_e64 s[38:39], s9, v16
	v_lshrrev_b32_e32 v13, 12, v14
	v_mbcnt_lo_u32_b32 v19, vcc_lo, 0
	v_mbcnt_lo_u32_b32 v20, s38, 0
	v_mbcnt_hi_u32_b32 v19, vcc_hi, v19
	v_mbcnt_hi_u32_b32 v20, s39, v20
	v_add_u32_e32 v21, v20, v19
	v_lshrrev_b32_e32 v18, 12, v16
	v_cndmask_b32_e32 v21, 0, v21, vcc
	v_addc_co_u32_e64 v19, s[40:41], v20, v19, vcc
	s_bcnt1_i32_b64 s5, vcc
	v_cmp_eq_u32_e32 vcc, 1, v13
	v_cndmask_b32_e64 v19, 0, v19, s[38:39]
	s_bcnt1_i32_b64 s30, s[38:39]
	v_cmp_eq_u32_e64 s[38:39], 1, v18
	v_mbcnt_lo_u32_b32 v20, vcc_lo, 0
	s_add_i32 s5, s30, s5
	v_mbcnt_hi_u32_b32 v20, vcc_hi, v20
	v_mbcnt_lo_u32_b32 v22, s38, 0
	v_mbcnt_hi_u32_b32 v22, s39, v22
	v_add_u32_e32 v20, s5, v20
	v_add_u32_e32 v23, v20, v22
	v_addc_co_u32_e64 v20, s[40:41], v20, v22, vcc
	s_bcnt1_i32_b64 s30, vcc
	v_cndmask_b32_e32 v21, v21, v23, vcc
	v_cndmask_b32_e64 v19, v19, v20, s[38:39]
	s_bcnt1_i32_b64 s38, s[38:39]
	s_add_i32 s30, s5, s30
	v_cmp_eq_u32_e32 vcc, 2, v13
	s_add_i32 s30, s30, s38
	v_cmp_eq_u32_e64 s[38:39], 2, v18
	v_mbcnt_lo_u32_b32 v20, vcc_lo, 0
	v_mbcnt_hi_u32_b32 v20, vcc_hi, v20
	v_mbcnt_lo_u32_b32 v22, s38, 0
	v_mbcnt_hi_u32_b32 v22, s39, v22
	v_add_u32_e32 v20, s30, v20
	v_add_u32_e32 v23, v20, v22
	v_addc_co_u32_e64 v20, s[40:41], v20, v22, vcc
	s_bcnt1_i32_b64 s40, vcc
	s_lshl_b32 s42, s30, 8
	v_cndmask_b32_e32 v21, v21, v23, vcc
	v_cndmask_b32_e64 v19, v19, v20, s[38:39]
	s_bcnt1_i32_b64 s38, s[38:39]
	s_add_i32 s30, s30, s40
	v_cmp_eq_u32_e32 vcc, 3, v13
	s_add_i32 s30, s30, s38
	v_cmp_eq_u32_e64 s[38:39], 3, v18
	v_mbcnt_lo_u32_b32 v13, vcc_lo, 0
	v_mbcnt_hi_u32_b32 v13, vcc_hi, v13
	v_mbcnt_lo_u32_b32 v18, s38, 0
	v_mbcnt_hi_u32_b32 v18, s39, v18
	v_add_u32_e32 v13, s30, v13
	v_add_u32_e32 v20, v13, v18
	v_cndmask_b32_e32 v20, v21, v20, vcc
	v_addc_co_u32_e32 v13, vcc, v13, v18, vcc
	v_cndmask_b32_e64 v13, v19, v13, s[38:39]
	v_lshl_add_u32 v18, v20, 3, s33
	v_lshl_add_u32 v13, v13, 3, s33
	ds_write_b64 v18, v[14:15]
	ds_write_b64 v13, v[16:17]
	ds_read_b128 v[14:17], v10
	s_lshl_b32 s30, s30, 16
	s_or_b32 s30, s42, s30
	s_or_b32 s5, s30, s5
	s_waitcnt lgkmcnt(0)
	v_and_b32_e32 v13, 0xffff, v14
	v_lshl_or_b32 v13, v16, 16, v13
	ds_write_b32 v11, v13
	v_mov_b32_e32 v16, v15
	v_mov_b32_e32 v13, s5
	v_cmp_eq_u32_e32 vcc, s3, v74
	s_add_i32 s3, s3, 1
	s_mov_b64 s[38:39], 0x400
	ds_write_b64 v12, v[16:17]
	v_cndmask_b32_e32 v9, v9, v13, vcc
	v_add_u32_e32 v12, 0x200, v12
	v_add_u32_e32 v11, 0x100, v11
	s_cmp_eq_u32 s3, 15
	v_lshl_add_u64 v[6:7], v[6:7], 0, s[38:39]
	s_cbranch_scc0 .LBB0_1726
	s_waitcnt vmcnt(0)
	v_cmp_gt_u32_e32 vcc, s9, v2
	v_cmp_gt_u32_e64 s[38:39], s9, v4
	s_add_u32 s3, s18, s76
	v_mbcnt_lo_u32_b32 v11, vcc_lo, 0
	v_mbcnt_lo_u32_b32 v12, s38, 0
	s_addc_u32 s5, s19, 0
	v_mbcnt_hi_u32_b32 v11, vcc_hi, v11
	v_mbcnt_hi_u32_b32 v12, s39, v12
	s_add_u32 s42, s3, 0x2800000
	v_lshrrev_b32_e32 v6, 12, v2
	v_add_u32_e32 v13, v12, v11
	s_addc_u32 s43, s5, 0
	v_lshrrev_b32_e32 v7, 12, v4
	v_cndmask_b32_e32 v13, 0, v13, vcc
	v_addc_co_u32_e64 v11, s[40:41], v12, v11, vcc
	s_bcnt1_i32_b64 s5, vcc
	v_cmp_eq_u32_e32 vcc, 1, v6
	v_cndmask_b32_e64 v11, 0, v11, s[38:39]
	s_bcnt1_i32_b64 s30, s[38:39]
	v_cmp_eq_u32_e64 s[38:39], 1, v7
	v_mbcnt_lo_u32_b32 v12, vcc_lo, 0
	s_add_i32 s5, s30, s5
	v_mbcnt_hi_u32_b32 v12, vcc_hi, v12
	v_mbcnt_lo_u32_b32 v14, s38, 0
	v_mbcnt_hi_u32_b32 v14, s39, v14
	v_add_u32_e32 v12, s5, v12
	v_add_u32_e32 v15, v12, v14
	v_addc_co_u32_e64 v12, s[40:41], v12, v14, vcc
	s_bcnt1_i32_b64 s30, vcc
	v_cndmask_b32_e32 v13, v13, v15, vcc
	v_cndmask_b32_e64 v11, v11, v12, s[38:39]
	s_bcnt1_i32_b64 s38, s[38:39]
	s_add_i32 s30, s5, s30
	v_cmp_eq_u32_e32 vcc, 2, v6
	s_add_i32 s30, s30, s38
	v_cmp_eq_u32_e64 s[38:39], 2, v7
	v_mbcnt_lo_u32_b32 v12, vcc_lo, 0
	v_mbcnt_hi_u32_b32 v12, vcc_hi, v12
	v_mbcnt_lo_u32_b32 v14, s38, 0
	v_mbcnt_hi_u32_b32 v14, s39, v14
	v_add_u32_e32 v12, s30, v12
	v_add_u32_e32 v15, v12, v14
	v_addc_co_u32_e64 v12, s[40:41], v12, v14, vcc
	s_bcnt1_i32_b64 s40, vcc
	s_lshl_b32 s44, s30, 8
	v_cndmask_b32_e32 v13, v13, v15, vcc
	v_cndmask_b32_e64 v11, v11, v12, s[38:39]
	s_bcnt1_i32_b64 s38, s[38:39]
	s_add_i32 s30, s30, s40
	v_cmp_eq_u32_e32 vcc, 3, v6
	s_add_i32 s30, s30, s38
	v_cmp_eq_u32_e64 s[38:39], 3, v7
	v_mbcnt_lo_u32_b32 v6, vcc_lo, 0
	v_mbcnt_hi_u32_b32 v6, vcc_hi, v6
	v_mbcnt_lo_u32_b32 v7, s38, 0
	v_mbcnt_hi_u32_b32 v7, s39, v7
	v_add_u32_e32 v6, s30, v6
	v_add_u32_e32 v12, v6, v7
	v_cndmask_b32_e32 v12, v13, v12, vcc
	v_addc_co_u32_e32 v6, vcc, v6, v7, vcc
	v_cndmask_b32_e64 v6, v11, v6, s[38:39]
	v_lshl_add_u32 v7, v12, 3, s33
	ds_write_b64 v7, v[2:3]
	v_lshl_add_u32 v2, v6, 3, s33
	ds_write_b64 v2, v[4:5]
	ds_read_b128 v[2:5], v10
	s_lshl_b32 s30, s30, 16
	s_or_b32 s30, s44, s30
	v_lshl_add_u32 v247, v74, 2, s94
	s_or_b32 s5, s30, s5
	s_waitcnt lgkmcnt(0)
	v_and_b32_e32 v2, 0xffff, v2
	v_lshl_or_b32 v2, v4, 16, v2
	ds_write_b32 v247, v2 offset:3840
	v_mov_b32_e32 v2, s5
	v_cmp_eq_u32_e32 vcc, 15, v74
	v_lshlrev_b32_e32 v224, 4, v74
	v_mov_b32_e32 v4, v3
	v_cndmask_b32_e32 v248, v9, v2, vcc
	v_bfe_u32 v2, v74, 2, 2
	v_ashrrev_i32_e32 v225, 31, v224
	s_add_u32 s46, s18, 0x26400000
	ds_write_b64 v8, v[4:5] offset:7680
	v_cmp_eq_u32_e64 s[38:39], v2, v1
	v_lshl_add_u64 v[2:3], s[42:43], 0, v[224:225]
	s_mov_b64 s[40:41], 0xe00000
	v_and_b32_e32 v4, 2, v74
	s_addc_u32 s47, s19, 0
	s_waitcnt vmcnt(0) lgkmcnt(0)
	v_lshl_add_u64 v[140:141], v[2:3], 0, s[40:41]
	v_cmp_eq_u32_e64 s[40:41], 0, v4
	v_and_b32_e32 v4, 1, v74
	v_ashrrev_i32_e32 v5, 3, v74
	s_add_u32 s6, s46, s6
	v_cmp_eq_u32_e64 s[42:43], 0, v4
	v_lshlrev_b32_e32 v4, 1, v1
	v_and_b32_e32 v5, -4, v5
	s_addc_u32 s7, s47, s7
	s_mov_b32 s3, 0
	v_cmp_eq_u32_e64 s[44:45], 0, v150
	v_and_or_b32 v152, v4, 2, v5
	v_lshl_add_u64 v[142:143], s[6:7], 0, v[224:225]
	v_lshl_add_u64 v[144:145], s[46:47], 0, v[224:225]
	v_mov_b32_e32 v183, 1.0
	v_cndmask_b32_e64 v184, 0, v183, s[38:39]
	v_cndmask_b32_e64 v185, 0, v184, s[40:41]
	v_cndmask_b32_e64 v186, v184, 0, s[40:41]
	v_cndmask_b32_e64 v174, 0, v185, s[42:43]
	v_cndmask_b32_e64 v175, v185, 0, s[42:43]
	v_cndmask_b32_e64 v176, 0, v186, s[42:43]
	v_cndmask_b32_e64 v177, v186, 0, s[42:43]
	v_mov_b32_e32 v178, 0x39800000
	v_mov_b32_e32 v179, 0x3d372713
	v_mov_b32_e32 v180, 0x3fcc422a
	v_mov_b32_e32 v181, 0xbfb8aa3b
	v_mov_b32_e32 v182, 0x3c800000
	v_readfirstlane_b32 s100, v140
	v_readfirstlane_b32 s101, v141
	s_branch .LBB0_1729

; #define PL_LOAD(RB, TAB, SE, BB) do { _Pragma("unroll") for (int _q = 0; _q < 16; ++_q) { \
;         const unsigned _pw = (unsigned)__builtin_amdgcn_readlane((int)(SE), (BB) * 8 + (_q >> 1)); const unsigned _idx = (_q & 1) ? (_pw >> 16) : (_pw & 0xffffu); \
;         (RB)[_q] = *(const v4u*)((TAB) + (size_t)_idx * 1024 + 16 * lane); } } while (0)
; __device__ __forceinline__ void peer_unit(Frame& F, const Args& a, int layer, int unit, bool last) {
;     ...
;             if (lt < 16) PL_LOAD(rb, U8, seL, lb);
.LBB0_1735:
	s_cmp_gt_i32 s59, 15
	s_cbranch_scc1 .Lpu_skip1
	s_lshl_b32 s46, s60, 3
	s_waitcnt lgkmcnt(0)
	v_readlane_b32 s47, v153, s46
	s_lshl_b32 s30, s47, 10
	s_and_b32 s30, s30, 0x3fffc00
	s_add_u32 vcc_lo, s100, s30
	s_addc_u32 vcc_hi, s101, 0
	global_load_dwordx4 v[4:7], v224, vcc
	s_bfe_u32 s30, s47, 0x100010
	s_lshl_b32 s30, s30, 10
	s_add_u32 vcc_lo, s100, s30
	s_addc_u32 vcc_hi, s101, 0
	global_load_dwordx4 v[8:11], v224, vcc
	s_or_b32 s30, s46, 1
	v_readlane_b32 s47, v153, s30
	s_lshl_b32 s30, s47, 10
	s_and_b32 s30, s30, 0x3fffc00
	s_add_u32 vcc_lo, s100, s30
	s_addc_u32 vcc_hi, s101, 0
	global_load_dwordx4 v[12:15], v224, vcc
	s_bfe_u32 s30, s47, 0x100010
	s_lshl_b32 s30, s30, 10
	s_add_u32 vcc_lo, s100, s30
	s_addc_u32 vcc_hi, s101, 0
	global_load_dwordx4 v[16:19], v224, vcc
	s_or_b32 s30, s46, 2
	v_readlane_b32 s47, v153, s30
	s_lshl_b32 s30, s47, 10
	s_and_b32 s30, s30, 0x3fffc00
	s_add_u32 vcc_lo, s100, s30
	s_addc_u32 vcc_hi, s101, 0
	global_load_dwordx4 v[20:23], v224, vcc
	s_bfe_u32 s30, s47, 0x100010
	s_lshl_b32 s30, s30, 10
	s_add_u32 vcc_lo, s100, s30
	s_addc_u32 vcc_hi, s101, 0
	global_load_dwordx4 v[24:27], v224, vcc
	s_or_b32 s30, s46, 3
	v_readlane_b32 s47, v153, s30
	s_lshl_b32 s30, s47, 10
	s_and_b32 s30, s30, 0x3fffc00
	s_add_u32 vcc_lo, s100, s30
	s_addc_u32 vcc_hi, s101, 0
	global_load_dwordx4 v[28:31], v224, vcc
	s_bfe_u32 s30, s47, 0x100010
	s_lshl_b32 s30, s30, 10
	s_add_u32 vcc_lo, s100, s30
	s_addc_u32 vcc_hi, s101, 0
	global_load_dwordx4 v[32:35], v224, vcc
	s_or_b32 s30, s46, 4
	v_readlane_b32 s47, v153, s30
	s_lshl_b32 s30, s47, 10
	s_and_b32 s30, s30, 0x3fffc00
	s_add_u32 vcc_lo, s100, s30
	s_addc_u32 vcc_hi, s101, 0
	global_load_dwordx4 v[36:39], v224, vcc
	s_bfe_u32 s30, s47, 0x100010
	s_lshl_b32 s30, s30, 10
	s_add_u32 vcc_lo, s100, s30
	s_addc_u32 vcc_hi, s101, 0
	global_load_dwordx4 v[40:43], v224, vcc
	s_or_b32 s30, s46, 5
	v_readlane_b32 s47, v153, s30
	s_lshl_b32 s30, s47, 10
	s_and_b32 s30, s30, 0x3fffc00
	s_add_u32 vcc_lo, s100, s30
	s_addc_u32 vcc_hi, s101, 0
	global_load_dwordx4 v[44:47], v224, vcc
	s_bfe_u32 s30, s47, 0x100010
	s_lshl_b32 s30, s30, 10
	s_add_u32 vcc_lo, s100, s30
	s_addc_u32 vcc_hi, s101, 0
	global_load_dwordx4 v[48:51], v224, vcc
	s_or_b32 s30, s46, 6
	v_readlane_b32 s47, v153, s30
	s_lshl_b32 s30, s47, 10
	s_and_b32 s30, s30, 0x3fffc00
	s_add_u32 vcc_lo, s100, s30
	s_addc_u32 vcc_hi, s101, 0
	global_load_dwordx4 v[52:55], v224, vcc
	s_bfe_u32 s30, s47, 0x100010
	s_lshl_b32 s30, s30, 10
	s_add_u32 vcc_lo, s100, s30
	s_addc_u32 vcc_hi, s101, 0
	global_load_dwordx4 v[56:59], v224, vcc
	s_or_b32 s30, s46, 7
	v_readlane_b32 s46, v153, s30
	s_lshl_b32 s30, s46, 10
	s_and_b32 s30, s30, 0x3fffc00
	s_add_u32 vcc_lo, s100, s30
	s_addc_u32 vcc_hi, s101, 0
	global_load_dwordx4 v[60:63], v224, vcc
	s_bfe_u32 s30, s46, 0x100010
	s_lshl_b32 s30, s30, 10
	s_add_u32 vcc_lo, s100, s30
	s_addc_u32 vcc_hi, s101, 0
	global_load_dwordx4 v[64:67], v224, vcc
	s_branch .Lpu_go1

; #define PL_LOAD(RB, TAB, SE, BB) do { _Pragma("unroll") for (int _q = 0; _q < 16; ++_q) { \
;         const unsigned _pw = (unsigned)__builtin_amdgcn_readlane((int)(SE), (BB) * 8 + (_q >> 1)); const unsigned _idx = (_q & 1) ? (_pw >> 16) : (_pw & 0xffffu); \
;         (RB)[_q] = *(const v4u*)((TAB) + (size_t)_idx * 1024 + 16 * lane); } } while (0)
; __device__ __forceinline__ void peer_unit(Frame& F, const Args& a, int layer, int unit, bool last) {
;     ...
;             if (lt < 16) PL_LOAD(ra, U8, seL, lb);
.LBB0_1756:
	s_cmp_gt_i32 s58, 15
	s_cbranch_scc1 .LBB0_1758
	s_lshl_b32 s47, s48, 3
	s_waitcnt lgkmcnt(0)
	v_readlane_b32 s56, v153, s47
	s_lshl_b32 s30, s56, 10
	s_and_b32 s30, s30, 0x3fffc00
	s_add_u32 vcc_lo, s100, s30
	s_addc_u32 vcc_hi, s101, 0
	global_load_dwordx4 v[72:75], v224, vcc
	s_bfe_u32 s30, s56, 0x100010
	s_lshl_b32 s30, s30, 10
	s_add_u32 vcc_lo, s100, s30
	s_addc_u32 vcc_hi, s101, 0
	global_load_dwordx4 v[76:79], v224, vcc
	s_or_b32 s30, s47, 1
	v_readlane_b32 s56, v153, s30
	s_lshl_b32 s30, s56, 10
	s_and_b32 s30, s30, 0x3fffc00
	s_add_u32 vcc_lo, s100, s30
	s_addc_u32 vcc_hi, s101, 0
	global_load_dwordx4 v[80:83], v224, vcc
	s_bfe_u32 s30, s56, 0x100010
	s_lshl_b32 s30, s30, 10
	s_add_u32 vcc_lo, s100, s30
	s_addc_u32 vcc_hi, s101, 0
	global_load_dwordx4 v[84:87], v224, vcc
	s_or_b32 s30, s47, 2
	v_readlane_b32 s56, v153, s30
	s_lshl_b32 s30, s56, 10
	s_and_b32 s30, s30, 0x3fffc00
	s_add_u32 vcc_lo, s100, s30
	s_addc_u32 vcc_hi, s101, 0
	global_load_dwordx4 v[88:91], v224, vcc
	s_bfe_u32 s30, s56, 0x100010
	s_lshl_b32 s30, s30, 10
	s_add_u32 vcc_lo, s100, s30
	s_addc_u32 vcc_hi, s101, 0
	global_load_dwordx4 v[92:95], v224, vcc
	s_or_b32 s30, s47, 3
	v_readlane_b32 s56, v153, s30
	s_lshl_b32 s30, s56, 10
	s_and_b32 s30, s30, 0x3fffc00
	s_add_u32 vcc_lo, s100, s30
	s_addc_u32 vcc_hi, s101, 0
	global_load_dwordx4 v[96:99], v224, vcc
	s_bfe_u32 s30, s56, 0x100010
	s_lshl_b32 s30, s30, 10
	s_add_u32 vcc_lo, s100, s30
	s_addc_u32 vcc_hi, s101, 0
	global_load_dwordx4 v[100:103], v224, vcc
	s_or_b32 s30, s47, 4
	v_readlane_b32 s56, v153, s30
	s_lshl_b32 s30, s56, 10
	s_and_b32 s30, s30, 0x3fffc00
	s_add_u32 vcc_lo, s100, s30
	s_addc_u32 vcc_hi, s101, 0
	global_load_dwordx4 v[104:107], v224, vcc
	s_bfe_u32 s30, s56, 0x100010
	s_lshl_b32 s30, s30, 10
	s_add_u32 vcc_lo, s100, s30
	s_addc_u32 vcc_hi, s101, 0
	global_load_dwordx4 v[108:111], v224, vcc
	s_or_b32 s30, s47, 5
	v_readlane_b32 s56, v153, s30
	s_lshl_b32 s30, s56, 10
	s_and_b32 s30, s30, 0x3fffc00
	s_add_u32 vcc_lo, s100, s30
	s_addc_u32 vcc_hi, s101, 0
	global_load_dwordx4 v[112:115], v224, vcc
	s_bfe_u32 s30, s56, 0x100010
	s_lshl_b32 s30, s30, 10
	s_add_u32 vcc_lo, s100, s30
	s_addc_u32 vcc_hi, s101, 0
	global_load_dwordx4 v[116:119], v224, vcc
	s_or_b32 s30, s47, 6
	v_readlane_b32 s56, v153, s30
	s_lshl_b32 s30, s56, 10
	s_and_b32 s30, s30, 0x3fffc00
	s_add_u32 vcc_lo, s100, s30
	s_addc_u32 vcc_hi, s101, 0
	global_load_dwordx4 v[120:123], v224, vcc
	s_bfe_u32 s30, s56, 0x100010
	s_lshl_b32 s30, s30, 10
	s_add_u32 vcc_lo, s100, s30
	s_addc_u32 vcc_hi, s101, 0
	global_load_dwordx4 v[124:127], v224, vcc
	s_or_b32 s30, s47, 7
	v_readlane_b32 s47, v153, s30
	s_lshl_b32 s30, s47, 10
	s_and_b32 s30, s30, 0x3fffc00
	s_add_u32 vcc_lo, s100, s30
	s_addc_u32 vcc_hi, s101, 0
	global_load_dwordx4 v[128:131], v224, vcc
	s_bfe_u32 s30, s47, 0x100010
	s_lshl_b32 s30, s30, 10
	s_add_u32 vcc_lo, s100, s30
	s_addc_u32 vcc_hi, s101, 0
	global_load_dwordx4 v[132:135], v224, vcc
	s_waitcnt vmcnt(16)
	s_branch .Lpu_go2
